# compress layer-2 dot-product loop (phase 4) software-pipelined: next 16 w2 loads requested before the current 16 are consumed
# speedup vs baseline: 1.0105x; 1.0064x over previous
.LBB0_401:
	v_add_co_u32_e32 v24, vcc, 0x100000, v14
	global_load_dword v23, v[14:15], off
	s_nop 0
	v_addc_co_u32_e32 v25, vcc, 0, v15, vcc
	v_add_co_u32_e32 v26, vcc, 0x200000, v14
	global_load_dword v30, v[24:25], off
	s_nop 0
	v_addc_co_u32_e32 v27, vcc, 0, v15, vcc
	v_add_co_u32_e32 v24, vcc, 0x300000, v14
	s_waitcnt vmcnt(1)
	v_add_f32_e32 v23, v16, v23
	v_addc_co_u32_e32 v25, vcc, 0, v15, vcc
	v_add_co_u32_e32 v28, vcc, 0x400000, v14
	global_load_dword v31, v[26:27], off
	global_load_dword v32, v[24:25], off
	v_addc_co_u32_e32 v29, vcc, 0, v15, vcc
	v_add_co_u32_e32 v24, vcc, 0x500000, v14
	s_waitcnt vmcnt(2)
	v_add_f32_e32 v23, v23, v30
	v_addc_co_u32_e32 v25, vcc, 0, v15, vcc
	v_add_co_u32_e32 v26, vcc, 0x600000, v14
	global_load_dword v28, v[28:29], off
	s_nop 0
	global_load_dword v29, v[24:25], off
	v_addc_co_u32_e32 v27, vcc, 0, v15, vcc
	v_add_co_u32_e32 v24, vcc, 0x700000, v14
	s_waitcnt vmcnt(3)
	v_add_f32_e32 v23, v23, v31
	v_addc_co_u32_e32 v25, vcc, 0, v15, vcc
	global_load_dword v26, v[26:27], off
	s_nop 0
	global_load_dword v24, v[24:25], off
	s_waitcnt vmcnt(4)
	v_add_f32_e32 v23, v23, v32
	v_add_co_u32_e32 v17, vcc, 0x200, v17
	s_xor_b64 s[34:35], vcc, -1
	s_and_b64 s[34:35], exec, s[34:35]
	v_lshl_add_u64 v[14:15], v[14:15], 0, s[16:17]
	s_waitcnt vmcnt(3)
	v_add_f32_e32 v23, v23, v28
	s_waitcnt vmcnt(2)
	v_add_f32_e32 v23, v23, v29
	s_or_b64 s[22:23], s[34:35], s[22:23]
	s_waitcnt vmcnt(1)
	v_add_f32_e32 v23, v23, v26
	s_waitcnt vmcnt(0)
	v_add_f32_e32 v23, v23, v24
	v_mul_f32_e32 v24, 0xbfb8aa3b, v23
	v_exp_f32_e32 v24, v24
	s_nop 0
	v_add_f32_e32 v24, 1.0, v24
	v_rcp_f32_e32 v24, v24
	s_nop 0
	v_mul_f32_e32 v23, v23, v24
	ds_write_b32 v4, v23
	v_add_u32_e32 v4, 0x800, v4
	s_andn2_b64 exec, exec, s[22:23]
	s_cbranch_execnz .LBB0_401
	s_or_b64 exec, exec, s[22:23]
	s_and_b64 s[22:23], s[18:19], exec
	s_cselect_b32 s23, s79, s39
	s_cselect_b32 s22, s78, s38
	s_waitcnt lgkmcnt(0)
	s_barrier
	global_load_dword v4, v21, s[22:23]
	s_cselect_b32 s23, s77, s37
	s_cselect_b32 s22, s76, s36
	v_lshl_add_u64 v[14:15], s[22:23], 0, v[12:13]
	s_mov_b64 s[22:23], 0
	v_mov_b32_e32 v16, v3
	v_lshl_add_u64 v[24:25], v[14:15], 0, s[22:23]
	global_load_dword v17, v[24:25], off
	global_load_dword v23, v[24:25], off offset:512
	global_load_dword v40, v[24:25], off offset:1024
	global_load_dword v41, v[24:25], off offset:1536
	global_load_dword v42, v[24:25], off offset:2048
	global_load_dword v43, v[24:25], off offset:2560
	global_load_dword v44, v[24:25], off offset:3072
	global_load_dword v45, v[24:25], off offset:3584
	v_add_co_u32_e32 v24, vcc, s3, v24
	s_add_u32 s22, s22, 0x2000
	s_nop 0
	v_addc_co_u32_e32 v25, vcc, 0, v25, vcc
	global_load_dword v46, v[24:25], off
	global_load_dword v47, v[24:25], off offset:512
	global_load_dword v48, v[24:25], off offset:1024
	global_load_dword v49, v[24:25], off offset:1536
	global_load_dword v50, v[24:25], off offset:2048
	global_load_dword v51, v[24:25], off offset:2560
	global_load_dword v52, v[24:25], off offset:3072
	global_load_dword v53, v[24:25], off offset:3584
	s_addc_u32 s23, s23, 0
.LBB0_403:
	v_lshl_add_u64 v[24:25], v[14:15], 0, s[22:23]
	global_load_dword v54, v[24:25], off
	global_load_dword v55, v[24:25], off offset:512
	global_load_dword v56, v[24:25], off offset:1024
	global_load_dword v57, v[24:25], off offset:1536
	global_load_dword v58, v[24:25], off offset:2048
	global_load_dword v59, v[24:25], off offset:2560
	global_load_dword v60, v[24:25], off offset:3072
	global_load_dword v61, v[24:25], off offset:3584
	v_add_co_u32_e32 v24, vcc, s3, v24
	s_add_u32 s22, s22, 0x2000
	s_nop 0
	v_addc_co_u32_e32 v25, vcc, 0, v25, vcc
	global_load_dword v62, v[24:25], off
	global_load_dword v63, v[24:25], off offset:512
	global_load_dword v64, v[24:25], off offset:1024
	global_load_dword v65, v[24:25], off offset:1536
	global_load_dword v66, v[24:25], off offset:2048
	global_load_dword v67, v[24:25], off offset:2560
	global_load_dword v68, v[24:25], off offset:3072
	global_load_dword v69, v[24:25], off offset:3584
	s_addc_u32 s23, s23, 0
	ds_read_b128 v[24:27], v16
	ds_read_b128 v[28:31], v16 offset:16
	ds_read_b128 v[32:35], v16 offset:32
	ds_read_b128 v[36:39], v16 offset:48
	v_add_u32_e32 v16, 64, v16
	s_waitcnt vmcnt(16) lgkmcnt(0)
	v_fmac_f32_e32 v4, v24, v17
	v_fmac_f32_e32 v4, v25, v23
	v_fmac_f32_e32 v4, v26, v40
	v_fmac_f32_e32 v4, v27, v41
	v_fmac_f32_e32 v4, v28, v42
	v_fmac_f32_e32 v4, v29, v43
	v_fmac_f32_e32 v4, v30, v44
	v_fmac_f32_e32 v4, v31, v45
	v_fmac_f32_e32 v4, v32, v46
	v_fmac_f32_e32 v4, v33, v47
	v_fmac_f32_e32 v4, v34, v48
	v_fmac_f32_e32 v4, v35, v49
	v_fmac_f32_e32 v4, v36, v50
	v_fmac_f32_e32 v4, v37, v51
	v_fmac_f32_e32 v4, v38, v52
	v_fmac_f32_e32 v4, v39, v53
	s_cmp_eq_u32 s22, 0x20000
	s_cbranch_scc1 .Lp4_tail
	v_lshl_add_u64 v[24:25], v[14:15], 0, s[22:23]
	global_load_dword v17, v[24:25], off
	global_load_dword v23, v[24:25], off offset:512
	global_load_dword v40, v[24:25], off offset:1024
	global_load_dword v41, v[24:25], off offset:1536
	global_load_dword v42, v[24:25], off offset:2048
	global_load_dword v43, v[24:25], off offset:2560
	global_load_dword v44, v[24:25], off offset:3072
	global_load_dword v45, v[24:25], off offset:3584
	v_add_co_u32_e32 v24, vcc, s3, v24
	s_add_u32 s22, s22, 0x2000
	s_nop 0
	v_addc_co_u32_e32 v25, vcc, 0, v25, vcc
	global_load_dword v46, v[24:25], off
	global_load_dword v47, v[24:25], off offset:512
	global_load_dword v48, v[24:25], off offset:1024
	global_load_dword v49, v[24:25], off offset:1536
	global_load_dword v50, v[24:25], off offset:2048
	global_load_dword v51, v[24:25], off offset:2560
	global_load_dword v52, v[24:25], off offset:3072
	global_load_dword v53, v[24:25], off offset:3584
	s_addc_u32 s23, s23, 0
	ds_read_b128 v[24:27], v16
	ds_read_b128 v[28:31], v16 offset:16
	ds_read_b128 v[32:35], v16 offset:32
	ds_read_b128 v[36:39], v16 offset:48
	v_add_u32_e32 v16, 64, v16
	s_waitcnt vmcnt(16) lgkmcnt(0)
	v_fmac_f32_e32 v4, v24, v54
	v_fmac_f32_e32 v4, v25, v55
	v_fmac_f32_e32 v4, v26, v56
	v_fmac_f32_e32 v4, v27, v57
	v_fmac_f32_e32 v4, v28, v58
	v_fmac_f32_e32 v4, v29, v59
	v_fmac_f32_e32 v4, v30, v60
	v_fmac_f32_e32 v4, v31, v61
	v_fmac_f32_e32 v4, v32, v62
	v_fmac_f32_e32 v4, v33, v63
	v_fmac_f32_e32 v4, v34, v64
	v_fmac_f32_e32 v4, v35, v65
	v_fmac_f32_e32 v4, v36, v66
	v_fmac_f32_e32 v4, v37, v67
	v_fmac_f32_e32 v4, v38, v68
	v_fmac_f32_e32 v4, v39, v69
	s_branch .LBB0_403
.Lp4_tail:
	ds_read_b128 v[24:27], v16
	ds_read_b128 v[28:31], v16 offset:16
	ds_read_b128 v[32:35], v16 offset:32
	ds_read_b128 v[36:39], v16 offset:48
	v_add_u32_e32 v16, 64, v16
	s_waitcnt vmcnt(0) lgkmcnt(0)
	v_fmac_f32_e32 v4, v24, v54
	v_fmac_f32_e32 v4, v25, v55
	v_fmac_f32_e32 v4, v26, v56
	v_fmac_f32_e32 v4, v27, v57
	v_fmac_f32_e32 v4, v28, v58
	v_fmac_f32_e32 v4, v29, v59
	v_fmac_f32_e32 v4, v30, v60
	v_fmac_f32_e32 v4, v31, v61
	v_fmac_f32_e32 v4, v32, v62
	v_fmac_f32_e32 v4, v33, v63
	v_fmac_f32_e32 v4, v34, v64
	v_fmac_f32_e32 v4, v35, v65
	v_fmac_f32_e32 v4, v36, v66
	v_fmac_f32_e32 v4, v37, v67
	v_fmac_f32_e32 v4, v38, v68
	v_fmac_f32_e32 v4, v39, v69
	v_add_u32_e32 v14, s20, v1
	v_ashrrev_i32_e32 v15, 1, v14
	v_mul_hi_i32 v14, v15, s2
	v_add_u32_e32 v14, v14, v15
	v_lshrrev_b32_e32 v16, 31, v14
	v_ashrrev_i32_e32 v14, 7, v14
	v_add_u32_e32 v14, v14, v16
	v_mul_lo_u32 v16, v14, s1
	v_sub_u32_e32 v16, v15, v16
	s_and_b64 s[22:23], s[18:19], s[6:7]
	ds_write_b32 v7, v4 offset:4096
	s_waitcnt lgkmcnt(0)
	s_barrier
	s_and_saveexec_b64 s[20:21], s[22:23]
	s_cbranch_execz .LBB0_399
	v_lshlrev_b32_e32 v4, 8, v16
	v_add_u32_e32 v24, v9, v4
	v_ashrrev_i32_e32 v25, 31, v24
	v_lshl_add_u64 v[24:25], v[24:25], 2, s[14:15]
	v_add_u32_e32 v4, v18, v4
	v_lshl_add_u64 v[26:27], v[4:5], 2, s[14:15]
	global_load_dword v24, v[24:25], off
	s_nop 0
	global_load_dword v25, v[26:27], off
	ds_read2_b32 v[26:27], v22 offset1:16
	s_waitcnt vmcnt(1)
	v_mov_b32_e32 v31, v24
	s_waitcnt vmcnt(0)
	v_mov_b32_e32 v30, v25
	s_waitcnt lgkmcnt(0)
	v_pk_mul_f32 v[28:29], v[24:25], v[26:27]
	v_pk_mul_f32 v[24:25], v[30:31], v[26:27]
	v_sub_f32_e32 v4, v28, v29
	v_add_f32_e32 v15, v24, v25
	v_cndmask_b32_e64 v4, v15, v4, s[8:9]
	s_branch .LBB0_399
